# attention unit: bias-table build issues its 7 bucket loads together and its 7 bias loads together (2 memory latencies instead of 14 serial)
# baseline (speedup 1.0000x reference)
.LBB0_296:
	s_or_b64 exec, exec, s[22:23]
	s_waitcnt vmcnt(3)
	ds_write_b128 v219, v[14:17]
	s_waitcnt vmcnt(1)
	ds_write_b128 v220, v[10:13]
	s_waitcnt vmcnt(0)
	v_lshlrev_b32_e32 v10, 16, v2
	v_and_or_b32 v10, v6, s36, v10
	v_lshrrev_b32_e32 v6, 16, v6
	v_and_or_b32 v2, v2, s37, v6
	v_add_u32_e32 v6, 0x9000, v221
	ds_write2_b32 v6, v10, v2 offset1:130
	v_lshlrev_b32_e32 v2, 16, v3
	v_lshrrev_b32_e32 v6, 16, v7
	v_and_or_b32 v2, v7, s36, v2
	v_and_or_b32 v3, v3, s37, v6
	v_add_u32_e32 v6, 0x9400, v221
	ds_write2_b32 v6, v2, v3 offset0:4 offset1:134
	v_lshlrev_b32_e32 v2, 16, v4
	v_lshrrev_b32_e32 v3, 16, v8
	v_and_or_b32 v2, v8, s36, v2
	v_and_or_b32 v3, v4, s37, v3
	v_add_u32_e32 v4, 0x9800, v221
	ds_write2_b32 v4, v2, v3 offset0:8 offset1:138
	v_lshlrev_b32_e32 v2, 16, v5
	v_lshrrev_b32_e32 v3, 16, v9
	v_and_or_b32 v2, v9, s36, v2
	v_and_or_b32 v3, v5, s37, v3
	v_add_u32_e32 v4, 0x9c00, v221
	s_add_i32 s28, s28, s25
	ds_write2_b32 v4, v2, v3 offset0:12 offset1:142
	v_add_u32_e32 v2, s28, v202
	v_ashrrev_i32_e32 v3, 31, v2
	v_lshlrev_b64 v[2:3], 9, v[2:3]
	v_lshl_add_u64 v[14:15], v[18:19], 0, v[2:3]
	global_load_dwordx4 v[2:5], v[14:15], off offset:768
	global_load_dwordx4 v[6:9], v[14:15], off offset:512
	global_load_dwordx4 v[10:13], v[14:15], off offset:256
	s_nop 0
	global_load_dwordx4 v[14:17], v[14:15], off
	s_waitcnt vmcnt(0)
	ds_write_b128 v222, v[14:17]
	ds_write_b128 v223, v[6:9]
	v_lshlrev_b32_e32 v6, 16, v2
	v_lshrrev_b32_e32 v7, 16, v10
	v_and_or_b32 v6, v10, s36, v6
	v_and_or_b32 v2, v2, s37, v7
	v_add_u32_e32 v7, 0x9000, v224
	ds_write2_b32 v7, v6, v2 offset1:130
	v_lshlrev_b32_e32 v2, 16, v3
	v_lshrrev_b32_e32 v6, 16, v11
	v_and_or_b32 v2, v11, s36, v2
	v_and_or_b32 v3, v3, s37, v6
	v_add_u32_e32 v6, 0x9400, v224
	ds_write2_b32 v6, v2, v3 offset0:4 offset1:134
	v_lshlrev_b32_e32 v2, 16, v4
	v_lshrrev_b32_e32 v3, 16, v12
	v_and_or_b32 v2, v12, s36, v2
	v_and_or_b32 v3, v4, s37, v3
	v_add_u32_e32 v4, 0x9800, v224
	ds_write2_b32 v4, v2, v3 offset0:8 offset1:138
	v_lshlrev_b32_e32 v2, 16, v5
	v_lshrrev_b32_e32 v3, 16, v13
	v_and_or_b32 v2, v13, s36, v2
	v_and_or_b32 v3, v5, s37, v3
	v_add_u32_e32 v4, 0x9c00, v224
	ds_write2_b32 v4, v2, v3 offset0:12 offset1:142
	s_mov_b64 s[6:7], exec
	v_readlane_b32 s8, v253, 31
	v_readlane_b32 s9, v253, 32
	s_and_b64 s[10:11], s[96:97], s[20:21]
	s_and_b64 s[8:9], s[8:9], s[64:65]
	s_and_b64 exec, s[6:7], s[40:41]
	global_load_ubyte v6, v[136:137], off
	s_and_b64 exec, s[6:7], s[58:59]
	global_load_ubyte v7, v[138:139], off
	s_and_b64 exec, s[6:7], s[0:1]
	global_load_ubyte v8, v[140:141], off
	s_and_b64 exec, s[6:7], s[56:57]
	global_load_ubyte v9, v[142:143], off
	s_and_b64 exec, s[6:7], s[54:55]
	global_load_ubyte v10, v[144:145], off
	s_and_b64 exec, s[6:7], s[8:9]
	global_load_ubyte v11, v[146:147], off
	s_and_b64 exec, s[6:7], s[10:11]
	global_load_ubyte v12, v[148:149], off
	s_mov_b64 exec, s[6:7]
	s_lshl_b32 s25, s24, 2
	v_mov_b32_e32 v13, 0xf149f2ca
	s_waitcnt vmcnt(0)
	v_lshl_or_b32 v6, v6, 5, s25
	v_lshlrev_b32_e32 v7, 3, v7
	v_or3_b32 v7, v7, v204, s24
	v_lshlrev_b32_e32 v7, 2, v7
	v_lshlrev_b32_e32 v8, 3, v8
	v_or3_b32 v8, v8, v206, s24
	v_lshlrev_b32_e32 v8, 2, v8
	v_lshlrev_b32_e32 v9, 3, v9
	v_add3_u32 v9, s24, v208, v9
	v_lshlrev_b32_e32 v9, 2, v9
	v_lshlrev_b32_e32 v10, 3, v10
	v_or3_b32 v10, v10, v210, s24
	v_lshlrev_b32_e32 v10, 2, v10
	v_lshlrev_b32_e32 v11, 3, v11
	v_add3_u32 v11, s24, v214, v11
	v_lshlrev_b32_e32 v11, 2, v11
	v_lshlrev_b32_e32 v12, 3, v12
	v_or3_b32 v12, v12, v216, s24
	v_lshlrev_b32_e32 v12, 2, v12
	s_and_b64 exec, s[6:7], s[40:41]
	global_load_dword v6, v6, s[68:69]
	s_and_b64 exec, s[6:7], s[58:59]
	global_load_dword v7, v7, s[68:69]
	s_and_b64 exec, s[6:7], s[0:1]
	global_load_dword v8, v8, s[68:69]
	s_and_b64 exec, s[6:7], s[56:57]
	global_load_dword v9, v9, s[68:69]
	s_and_b64 exec, s[6:7], s[54:55]
	global_load_dword v10, v10, s[68:69]
	s_and_b64 exec, s[6:7], s[8:9]
	global_load_dword v11, v11, s[68:69]
	s_and_b64 exec, s[6:7], s[10:11]
	global_load_dword v12, v12, s[68:69]
	s_mov_b64 exec, s[6:7]
	s_waitcnt vmcnt(0)
	v_mul_f32_e32 v6, 0x3fb8aa3b, v6
	v_mul_f32_e32 v7, 0x3fb8aa3b, v7
	v_mul_f32_e32 v8, 0x3fb8aa3b, v8
	v_mul_f32_e32 v9, 0x3fb8aa3b, v9
	v_mul_f32_e32 v10, 0x3fb8aa3b, v10
	v_mul_f32_e32 v11, 0x3fb8aa3b, v11
	v_mul_f32_e32 v12, 0x3fb8aa3b, v12
	v_cndmask_b32_e64 v14, v13, v6, s[40:41]
	v_cndmask_b32_e64 v15, v13, v7, s[58:59]
	v_cndmask_b32_e64 v16, v13, v8, s[0:1]
	v_cndmask_b32_e64 v17, v13, v9, s[56:57]
	v_cndmask_b32_e64 v18, v13, v10, s[54:55]
	v_cndmask_b32_e64 v19, v13, v11, s[8:9]
	v_cndmask_b32_e64 v20, v13, v12, s[10:11]
	ds_write_b32 v203, v14
	ds_write_b32 v205, v15
	ds_write_b32 v207, v16
	ds_write_b32 v209, v17
	ds_write_b32 v211, v18
	s_and_b64 exec, s[6:7], s[64:65]
	ds_write_b32 v215, v19
	s_and_b64 exec, s[6:7], s[96:97]
	ds_write_b32 v1, v20
	s_mov_b64 exec, s[6:7]
	s_lshl_b32 s25, s3, 6
	s_lshl_b32 s3, s3, 2
	v_readlane_b32 s4, v253, 8
	v_mov_b32_e32 v2, s3
	v_readlane_b32 s16, v253, 20
	v_readlane_b32 s17, v253, 21
	s_waitcnt lgkmcnt(0)
	s_barrier
	s_cmp_lg_u32 s2, 0
	s_mov_b32 s3, 0
	s_nop 0
	global_load_dword v2, v2, s[16:17]
	s_mov_b64 s[80:81], -1
	s_cselect_b64 s[78:79], -1, 0
	s_lshl_b32 s60, s25, 1
	v_readlane_b32 s5, v253, 9
	v_readlane_b32 s6, v253, 10
	v_readlane_b32 s7, v253, 11
	v_readlane_b32 s8, v253, 12
	v_readlane_b32 s9, v253, 13
	v_readlane_b32 s10, v253, 14
	v_readlane_b32 s11, v253, 15
	v_readlane_b32 s12, v253, 16
	v_readlane_b32 s13, v253, 17
	v_readlane_b32 s14, v253, 18
	v_readlane_b32 s15, v253, 19
	v_readlane_b32 s18, v253, 22
	v_readlane_b32 s19, v253, 23
	s_waitcnt vmcnt(0)
	v_mul_f32_e32 v225, 0x3fb8aa3b, v2
	v_max_f32_e32 v226, 0xf149f2ca, v225
	s_branch .LBB0_317
